# phase 10 moe_tables: tile tables via 32-lane DPP prefix sum instead of a one-thread loop over experts; on top of v40
# speedup vs baseline: 1.0129x; 1.0073x over previous
; #define LAS __attribute__((address_space(3)))
; __device__ __forceinline__ void moe_tables(const int* ECNT, LAS unsigned char* lds, int tid) {
;     LAS int* totp = (LAS int*)lds;
;     LAS int* tile_e = (LAS int*)(lds + TILE_OFF); LAS int* ntl = tile_e + 160; LAS int* pstart = (LAS int*)(lds + TILE_OFF + 1024);
;     if (tid < 32) { const int tot = ECNT[16 * tid]; totp[tid] = tot; ((LAS int*)(lds + TILE_OFF + 1280))[tid] = tot; }
;     __syncthreads();
;     if (tid == 0) { int ps = 0, nt = 0;
;         for (int e = 0; e < NE; ++e) { const int c = totp[e]; const int npad = (c + 255) >> 8; pstart[e] = ps; for (int k = 0; k < npad; ++k) { if (nt < 160) tile_e[nt] = e; ++nt; } ps += npad * 256; }
;         *ntl = nt < 160 ? nt : 160; }
;     __syncthreads();
; }
.LBB0_1017:
	s_or_b64 exec, exec, s[2:3]
	s_mov_b32 s10, 0
	v_cmp_gt_u32_e32 vcc, 32, v0
	s_waitcnt lgkmcnt(0)
	s_barrier
	s_and_saveexec_b64 s[2:3], vcc
	s_cbranch_execz .LBB0_2139
	v_lshlrev_b32_e32 v1, 2, v0
	ds_read_b32 v2, v1
	s_waitcnt lgkmcnt(0)
	v_add_u32_e32 v2, 0xff, v2
	v_ashrrev_i32_e32 v2, 8, v2
	v_mov_b32_e32 v3, v2
	s_nop 1
	v_add_u32_dpp v3, v3, v3 row_shr:1 row_mask:0xf bank_mask:0xf bound_ctrl:0
	s_nop 1
	v_add_u32_dpp v3, v3, v3 row_shr:2 row_mask:0xf bank_mask:0xf bound_ctrl:0
	s_nop 1
	v_add_u32_dpp v3, v3, v3 row_shr:4 row_mask:0xf bank_mask:0xf bound_ctrl:0
	s_nop 1
	v_add_u32_dpp v3, v3, v3 row_shr:8 row_mask:0xf bank_mask:0xf bound_ctrl:0
	s_nop 0
	v_readlane_b32 s4, v3, 15
	v_cmp_lt_u32_e32 vcc, 15, v0
	s_nop 1
	v_mov_b32_e32 v4, s4
	s_nop 0
	v_cndmask_b32_e32 v4, 0, v4, vcc
	v_add_u32_e32 v3, v3, v4
	v_sub_u32_e32 v4, v3, v2
	v_lshlrev_b32_e32 v5, 8, v4
	v_add_u32_e32 v6, 0x27000, v1
	ds_write_b32 v6, v5
	s_nop 0
	v_readlane_b32 s5, v3, 31
	s_mov_b64 s[14:15], exec
	v_mov_b32_e32 v5, 0
.Lmt_loop:
	v_cmp_lt_i32_e32 vcc, v5, v2
	s_cbranch_vccz .Lmt_done
	s_and_b64 exec, exec, vcc
	v_add_u32_e32 v6, v4, v5
	v_cmp_gt_u32_e32 vcc, 0xa0, v6
	s_and_b64 exec, exec, vcc
	v_lshlrev_b32_e32 v7, 2, v6
	v_add_u32_e32 v7, 0x26c00, v7
	ds_write_b32 v7, v0
	s_mov_b64 exec, s[14:15]
	v_add_u32_e32 v5, 1, v5
	s_branch .Lmt_loop
.Lmt_done:
	s_mov_b64 exec, s[14:15]
	s_min_i32 s5, s5, 0xa0
	v_mov_b32_e32 v5, s5
	v_mov_b32_e32 v6, 0x26e80
	v_cmp_eq_u32_e32 vcc, 0, v0
	s_and_b64 exec, exec, vcc
	ds_write_b32 v6, v5
